# zfirst
# baseline (speedup 1.0000x reference)
_Z11attn_kernelILi4EEvPKfS1_S1_S1_S1_S1_PKcPf:
	s_load_dwordx2 s[24:25], s[0:1], 0x30
	s_load_dwordx8 s[8:15], s[0:1], 0x0
	s_load_dwordx4 s[16:19], s[0:1], 0x20
	v_lshrrev_b32_e32 v63, 6, v0
	v_and_b32_e32 v57, 15, v0
	v_bfe_u32 v1, v0, 4, 2
	v_lshrrev_b32_e32 v2, 2, v57
	v_mul_u32_u24_e32 v4, 3, v1
	v_mul_u32_u24_e32 v2, 3, v2
	v_mad_u32_u24 v4, v63, 12, v4
	v_mad_u32_u24 v2, v63, 12, v2
	v_lshlrev_b32_e32 v4, 2, v4
	v_lshlrev_b32_e32 v2, 2, v2
	v_and_b32_e32 v104, 63, v0
	v_lshlrev_b32_e32 v60, 5, v57
	v_lshlrev_b32_e32 v58, 3, v1
	v_add_u32_e32 v3, v60, v58
	v_lshrrev_b32_e32 v56, 4, v0
	v_lshlrev_b32_e32 v54, 4, v57
	v_mov_b32_e32 v59, 0
	s_movk_i32 s4, 0xe0
	v_cmp_gt_u32_e64 s[4:5], s4, v0
	s_lshl_b32 s26, s2, 8
	s_lshl_b32 s27, s2, 9
	s_mul_i32 s28, s2, 14
	s_add_u32 s26, s26, 0x164000
	s_add_u32 s27, s27, 0x80000
	s_add_u32 s20, s26, 0xc0
	v_lshlrev_b32_e32 v5, 2, v57
	v_lshlrev_b32_e32 v147, 6, v57
	v_add_u32_e32 v2, s26, v2
	v_add_u32_e32 v4, s26, v4
	v_add_u32_e32 v3, s27, v3
	v_mul_u32_u24_e32 v156, 0x140, v1
	s_movk_i32 s21, 0x500
	v_mad_u32_u24 v156, v63, s21, v156
	v_lshl_or_b32 v156, v57, 2, v156
	v_add_u32_e32 v156, 0x1c00, v156
	v_lshlrev_b32_e32 v157, 5, v56
	v_cmp_gt_u32_e32 vcc, 3, v57
	v_add_u32_e32 v158, 4, v57
	v_lshlrev_b32_e32 v159, 2, v57
	s_movk_i32 s21, 0x50
	v_cndmask_b32_e32 v158, 4, v158, vcc
	v_mad_u32_u24 v159, v56, s21, v159
	v_lshl_add_u32 v158, v158, 2, v157
	v_mul_u32_u24_e32 v250, 0x50, v56
	v_or_b32_e32 v250, 0x3800, v250
	v_lshl_add_u32 v251, v57, 1, v250
	v_mul_u32_u24_e32 v252, 0x50, v57
	v_lshl_add_u32 v252, v58, 1, v252
	v_lshlrev_b32_e32 v253, 2, v57
	v_and_b32_e32 v254, 0xc0, v0
	v_lshlrev_b32_e32 v255, 11, v1
	v_or3_b32 v253, v253, v254, v255
	v_add_u32_e32 v254, s28, v56
	v_lshl_add_u32 v254, v254, 9, v54
	v_lshl_or_b32 v255, v56, 9, v54
	s_movk_i32 s6, 0x140
	v_cmp_gt_u32_e32 vcc, s6, v0
	v_lshlrev_b32_e32 v22, 2, v0
	v_mov_b32_e32 v23, 0
	s_and_saveexec_b64 s[6:7], vcc
	ds_write_b32 v22, v23 offset:14336
	s_or_b64 exec, exec, s[6:7]
	v_cmp_gt_u32_e32 vcc, 64, v0
	s_and_saveexec_b64 s[6:7], vcc
	ds_write_b32 v22, v23 offset:15360
	s_or_b64 exec, exec, s[6:7]
	v_mov_b32_e32 v45, 0xc9c35000
	s_mov_b32 s30, 0x3db8aa3b
	s_mov_b32 s31, 0x3db8aa3b
	v_mov_b32_e32 v121, 0x3fb8aa3b
	v_mov_b32_e32 v35, 0
	v_mov_b32_e32 v44, v45
	s_waitcnt lgkmcnt(0)
	global_load_dwordx3 v[80:82], v2, s[24:25]
	global_load_dwordx3 v[84:86], v4, s[24:25]
	global_load_dwordx2 v[64:65], v3, s[24:25]
	s_load_dword s3, s[24:25], s20
	s_add_u32 s22, s24, 0x160000
	s_addc_u32 s23, s25, 0
	v_cndmask_b32_e64 v62, 13, v56, s[4:5]
	v_add_u32_e32 v3, s28, v62
	v_mad_u32_u24 v144, v3, 36, v5
	v_mad_u32_u24 v146, v3, 12, v5
	v_add_u32_e32 v145, -36, v146
	v_add_u32_e32 v146, -48, v146
	v_lshl_or_b32 v147, v63, 10, v147
	v_lshl_or_b32 v147, v1, 4, v147
	v_or_b32_e32 v148, 0x1000, v147
	v_lshlrev_b32_e32 v149, 4, v104
	v_lshlrev_b32_e32 v150, 9, v3
	v_add_u32_e32 v150, v150, v54
	v_and_b32_e32 v87, 3, v57
	v_lshlrev_b32_e32 v87, 4, v87
	v_lshl_or_b32 v87, v1, 6, v87
	v_lshlrev_b32_e32 v88, 3, v57
	s_add_u32 s26, s24, 0x100000
	s_addc_u32 s27, s25, 0
	s_add_u32 s28, s24, 0x140000
	s_addc_u32 s29, s25, 0
	s_waitcnt lgkmcnt(0)
	s_bitcmp0_b32 s3, 1
	s_cselect_b64 s[20:21], -1, 0
	s_cbranch_scc1 .LBB1_16
	v_bfe_u32 v46, s3, v57, 1
	v_cmp_eq_u32_e32 vcc, 0, v46
	s_nop 1
	v_cndmask_b32_e32 v47, 0, v45, vcc
	v_cndmask_b32_e64 v55, 1.0, 0, vcc
	s_nop 0
	v_mov_b32_dpp v34, v47 row_newbcast:0 row_mask:0xf bank_mask:0xf bound_ctrl:1
	v_mov_b32_dpp v36, v47 row_newbcast:2 row_mask:0xf bank_mask:0xf bound_ctrl:1
	v_mov_b32_dpp v37, v47 row_newbcast:3 row_mask:0xf bank_mask:0xf bound_ctrl:1
	v_mov_b32_dpp v22, v47 row_newbcast:4 row_mask:0xf bank_mask:0xf bound_ctrl:1
	v_mov_b32_dpp v23, v47 row_newbcast:5 row_mask:0xf bank_mask:0xf bound_ctrl:1
	v_mov_b32_dpp v24, v47 row_newbcast:6 row_mask:0xf bank_mask:0xf bound_ctrl:1
	v_mov_b32_dpp v25, v47 row_newbcast:7 row_mask:0xf bank_mask:0xf bound_ctrl:1
	v_mov_b32_dpp v38, v47 row_newbcast:8 row_mask:0xf bank_mask:0xf bound_ctrl:1
	v_mov_b32_dpp v39, v47 row_newbcast:9 row_mask:0xf bank_mask:0xf bound_ctrl:1
	v_mov_b32_dpp v40, v47 row_newbcast:10 row_mask:0xf bank_mask:0xf bound_ctrl:1
	v_mov_b32_dpp v41, v47 row_newbcast:11 row_mask:0xf bank_mask:0xf bound_ctrl:1
	v_mov_b32_dpp v42, v47 row_newbcast:12 row_mask:0xf bank_mask:0xf bound_ctrl:1
	v_mov_b32_dpp v43, v47 row_newbcast:13 row_mask:0xf bank_mask:0xf bound_ctrl:1
	s_waitcnt vmcnt(1)
	v_lshl_add_u32 v72, v80, 9, v87
	v_lshl_add_u32 v73, v81, 9, v87
	v_lshl_add_u32 v74, v82, 9, v87
	global_load_dwordx4 v[50:53], v72, s[24:25]
	global_load_dwordx4 v[46:49], v72, s[24:25] offset:256
	global_load_dwordx4 v[14:17], v73, s[24:25]
	global_load_dwordx4 v[10:13], v73, s[24:25] offset:256
	global_load_dwordx4 v[6:9], v74, s[24:25]
	global_load_dwordx4 v[2:5], v74, s[24:25] offset:256
	v_lshl_add_u32 v75, v84, 8, v54
	v_lshl_add_u32 v78, v84, 7, v88
	v_lshl_add_u32 v76, v85, 8, v54
	v_lshl_add_u32 v79, v85, 7, v88
	v_lshl_add_u32 v77, v86, 8, v54
	v_lshl_add_u32 v80, v86, 7, v88
	global_load_dwordx4 v[30:33], v75, s[26:27]
	global_load_dwordx2 v[70:71], v78, s[28:29]
	global_load_dwordx4 v[26:29], v76, s[26:27]
	global_load_dwordx2 v[66:67], v79, s[28:29]
	global_load_dwordx4 v[18:21], v77, s[26:27]
	global_load_dwordx2 v[68:69], v80, s[28:29]
	s_mov_b32 exec_lo, 0x1ff01ff
	s_mov_b32 exec_hi, 0x1ff01ff
	global_load_dword v120, v144, s[10:11]
	s_mov_b32 exec_lo, 0xe000e00
	s_mov_b32 exec_hi, 0xe000e00
	global_load_dword v120, v145, s[12:13]
	s_mov_b32 exec_lo, 0x70007000
	s_mov_b32 exec_hi, 0x70007000
	global_load_dword v120, v146, s[14:15]
	s_mov_b64 exec, -1
	global_load_dwordx4 v[124:127], v147, s[22:23]
	global_load_dwordx4 v[128:131], v148, s[22:23]
	s_mov_b32 exec_hi, 0
	global_load_dwordx4 v[132:135], v149, s[16:17]
	s_mov_b32 exec_hi, -1
	s_mov_b32 exec_lo, 0
	global_load_dwordx4 v[132:135], v149, s[18:19] offset:-512
	s_mov_b32 exec_lo, -1
	global_load_dwordx4 v[136:139], v150, s[8:9]
	global_load_dwordx4 v[140:143], v150, s[8:9] offset:256
	v_mov_b32_e32 v75, 0
	v_mov_b32_e32 v79, 0
	v_mov_b32_e32 v83, 0
	s_waitcnt vmcnt(20)
	v_mfma_f32_16x16x32_fp8_fp8 v[160:163], v[50:51], v[64:65], v[34:37]
	v_mfma_f32_16x16x32_fp8_fp8 v[164:167], v[52:53], v[64:65], v[22:25]
	s_waitcnt vmcnt(19)
	v_mfma_f32_16x16x32_fp8_fp8 v[168:171], v[46:47], v[64:65], v[38:41]
	v_mfma_f32_16x16x32_fp8_fp8 v[172:175], v[48:49], v[64:65], v[42:45]
	s_nop 3
	v_max3_f32 v86, v160, v161, v162
	v_max3_f32 v87, v163, v164, v165
	v_max3_f32 v88, v166, v167, v168
	v_max3_f32 v89, v169, v170, v171
	v_max3_f32 v86, v86, v172, v173
	v_max3_f32 v87, v87, v88, v89
	v_max_f32_e32 v96, v86, v87
	v_mul_f32_e32 v98, 0xbdb8aa3b, v96
	v_pk_fma_f32 v[208:209], v[160:161], s[30:31], v[98:99] op_sel_hi:[1,1,0]
	v_pk_fma_f32 v[210:211], v[162:163], s[30:31], v[98:99] op_sel_hi:[1,1,0]
	v_pk_fma_f32 v[212:213], v[164:165], s[30:31], v[98:99] op_sel_hi:[1,1,0]
	v_pk_fma_f32 v[214:215], v[166:167], s[30:31], v[98:99] op_sel_hi:[1,1,0]
	v_pk_fma_f32 v[216:217], v[168:169], s[30:31], v[98:99] op_sel_hi:[1,1,0]
	v_pk_fma_f32 v[218:219], v[170:171], s[30:31], v[98:99] op_sel_hi:[1,1,0]
	v_pk_fma_f32 v[220:221], v[172:173], s[30:31], v[98:99] op_sel_hi:[1,1,0]
	v_exp_f32_e32 v208, v208
	v_exp_f32_e32 v209, v209
	v_exp_f32_e32 v210, v210
	v_exp_f32_e32 v211, v211
	v_exp_f32_e32 v212, v212
	v_exp_f32_e32 v213, v213
	v_exp_f32_e32 v214, v214
	v_exp_f32_e32 v215, v215
	v_exp_f32_e32 v216, v216
	v_exp_f32_e32 v217, v217
	v_exp_f32_e32 v218, v218
	v_exp_f32_e32 v219, v219
	v_exp_f32_e32 v220, v220
	v_exp_f32_e32 v221, v221
	s_waitcnt vmcnt(18)
	v_mfma_f32_16x16x32_fp8_fp8 v[176:179], v[14:15], v[64:65], v[34:37]
	v_mfma_f32_16x16x32_fp8_fp8 v[180:183], v[16:17], v[64:65], v[22:25]
	s_waitcnt vmcnt(17)
	v_mfma_f32_16x16x32_fp8_fp8 v[184:187], v[10:11], v[64:65], v[38:41]
	v_mfma_f32_16x16x32_fp8_fp8 v[188:191], v[12:13], v[64:65], v[42:45]
	v_pk_add_f32 v[86:87], v[208:209], v[210:211]
	v_pk_add_f32 v[88:89], v[212:213], v[214:215]
	v_pk_add_f32 v[90:91], v[216:217], v[218:219]
	v_pk_mul_f32 v[92:93], v[208:209], v[160:161]
	v_pk_mul_f32 v[94:95], v[210:211], v[162:163]
	v_pk_add_f32 v[86:87], v[86:87], v[220:221]
	v_pk_add_f32 v[88:89], v[88:89], v[90:91]
	v_pk_fma_f32 v[92:93], v[212:213], v[164:165], v[92:93]
	v_pk_fma_f32 v[94:95], v[214:215], v[166:167], v[94:95]
	v_pk_add_f32 v[86:87], v[86:87], v[88:89]
	v_pk_fma_f32 v[92:93], v[216:217], v[168:169], v[92:93]
	v_pk_fma_f32 v[94:95], v[218:219], v[170:171], v[94:95]
	v_add_f32_e32 v86, v86, v87
	v_pk_fma_f32 v[92:93], v[220:221], v[172:173], v[92:93]
	v_rcp_f32_e32 v87, v86
	v_pk_add_f32 v[92:93], v[92:93], v[94:95]
	v_mul_f32_e32 v87, v55, v87
	v_add_f32_e32 v92, v92, v93
	v_mul_f32_e32 v107, v86, v87
	v_mul_f32_e32 v92, v92, v87
	v_mul_f32_e32 v100, 0x43800000, v87
	v_mul_f32_e32 v103, 0x3d800000, v92
	v_max3_f32 v86, v176, v177, v178
	v_max3_f32 v87, v179, v180, v181
	v_max3_f32 v88, v182, v183, v184
	v_max3_f32 v89, v185, v186, v187
	v_max3_f32 v86, v86, v188, v189
	v_max3_f32 v87, v87, v88, v89
	v_max_f32_e32 v96, v86, v87
	v_mul_f32_e32 v98, 0xbdb8aa3b, v96
	v_pk_fma_f32 v[222:223], v[176:177], s[30:31], v[98:99] op_sel_hi:[1,1,0]
	v_pk_fma_f32 v[224:225], v[178:179], s[30:31], v[98:99] op_sel_hi:[1,1,0]
	v_pk_fma_f32 v[226:227], v[180:181], s[30:31], v[98:99] op_sel_hi:[1,1,0]
	v_pk_fma_f32 v[228:229], v[182:183], s[30:31], v[98:99] op_sel_hi:[1,1,0]
	v_pk_fma_f32 v[230:231], v[184:185], s[30:31], v[98:99] op_sel_hi:[1,1,0]
	v_pk_fma_f32 v[232:233], v[186:187], s[30:31], v[98:99] op_sel_hi:[1,1,0]
	v_pk_fma_f32 v[234:235], v[188:189], s[30:31], v[98:99] op_sel_hi:[1,1,0]
	v_exp_f32_e32 v222, v222
	v_exp_f32_e32 v223, v223
	v_exp_f32_e32 v224, v224
	v_exp_f32_e32 v225, v225
	v_exp_f32_e32 v226, v226
	v_exp_f32_e32 v227, v227
	v_exp_f32_e32 v228, v228
	v_exp_f32_e32 v229, v229
	v_exp_f32_e32 v230, v230
	v_exp_f32_e32 v231, v231
	v_exp_f32_e32 v232, v232
	v_exp_f32_e32 v233, v233
	v_exp_f32_e32 v234, v234
	v_exp_f32_e32 v235, v235
	s_waitcnt vmcnt(16)
	v_mfma_f32_16x16x32_fp8_fp8 v[192:195], v[6:7], v[64:65], v[34:37]
	v_mfma_f32_16x16x32_fp8_fp8 v[196:199], v[8:9], v[64:65], v[22:25]
	s_waitcnt vmcnt(15)
	v_mfma_f32_16x16x32_fp8_fp8 v[200:203], v[2:3], v[64:65], v[38:41]
	v_mfma_f32_16x16x32_fp8_fp8 v[204:207], v[4:5], v[64:65], v[42:45]
	v_pk_add_f32 v[86:87], v[222:223], v[224:225]
	v_pk_add_f32 v[88:89], v[226:227], v[228:229]
	v_pk_add_f32 v[90:91], v[230:231], v[232:233]
	v_pk_mul_f32 v[92:93], v[222:223], v[176:177]
	v_pk_mul_f32 v[94:95], v[224:225], v[178:179]
	v_pk_add_f32 v[86:87], v[86:87], v[234:235]
	v_pk_add_f32 v[88:89], v[88:89], v[90:91]
	v_pk_fma_f32 v[92:93], v[226:227], v[180:181], v[92:93]
	v_pk_fma_f32 v[94:95], v[228:229], v[182:183], v[94:95]
	v_pk_add_f32 v[86:87], v[86:87], v[88:89]
	v_pk_fma_f32 v[92:93], v[230:231], v[184:185], v[92:93]
	v_pk_fma_f32 v[94:95], v[232:233], v[186:187], v[94:95]
	v_add_f32_e32 v86, v86, v87
	v_pk_fma_f32 v[92:93], v[234:235], v[188:189], v[92:93]
	v_rcp_f32_e32 v87, v86
	v_pk_add_f32 v[92:93], v[92:93], v[94:95]
	v_mul_f32_e32 v87, v55, v87
	v_add_f32_e32 v92, v92, v93
	v_mul_f32_e32 v108, v86, v87
	v_mul_f32_e32 v92, v92, v87
	v_mul_f32_e32 v101, 0x43800000, v87
	v_mul_f32_e32 v105, 0x3d800000, v92
	v_max3_f32 v86, v192, v193, v194
	v_max3_f32 v87, v195, v196, v197
	v_max3_f32 v88, v198, v199, v200
	v_max3_f32 v89, v201, v202, v203
	v_max3_f32 v86, v86, v204, v205
	v_max3_f32 v87, v87, v88, v89
	v_max_f32_e32 v96, v86, v87
	v_mul_f32_e32 v98, 0xbdb8aa3b, v96
	v_pk_fma_f32 v[236:237], v[192:193], s[30:31], v[98:99] op_sel_hi:[1,1,0]
	v_pk_fma_f32 v[238:239], v[194:195], s[30:31], v[98:99] op_sel_hi:[1,1,0]
	v_pk_fma_f32 v[240:241], v[196:197], s[30:31], v[98:99] op_sel_hi:[1,1,0]
	v_pk_fma_f32 v[242:243], v[198:199], s[30:31], v[98:99] op_sel_hi:[1,1,0]
	v_pk_fma_f32 v[244:245], v[200:201], s[30:31], v[98:99] op_sel_hi:[1,1,0]
	v_pk_fma_f32 v[246:247], v[202:203], s[30:31], v[98:99] op_sel_hi:[1,1,0]
	v_pk_fma_f32 v[248:249], v[204:205], s[30:31], v[98:99] op_sel_hi:[1,1,0]
	v_exp_f32_e32 v236, v236
	v_exp_f32_e32 v237, v237
	v_exp_f32_e32 v238, v238
	v_exp_f32_e32 v239, v239
	v_exp_f32_e32 v240, v240
	v_exp_f32_e32 v241, v241
	v_exp_f32_e32 v242, v242
	v_exp_f32_e32 v243, v243
	v_exp_f32_e32 v244, v244
	v_exp_f32_e32 v245, v245
	v_exp_f32_e32 v246, v246
	v_exp_f32_e32 v247, v247
	v_exp_f32_e32 v248, v248
	v_exp_f32_e32 v249, v249
	v_pk_add_f32 v[86:87], v[236:237], v[238:239]
	v_pk_add_f32 v[88:89], v[240:241], v[242:243]
	v_pk_add_f32 v[90:91], v[244:245], v[246:247]
	v_pk_mul_f32 v[92:93], v[236:237], v[192:193]
	v_pk_mul_f32 v[94:95], v[238:239], v[194:195]
	v_pk_add_f32 v[86:87], v[86:87], v[248:249]
	v_pk_add_f32 v[88:89], v[88:89], v[90:91]
	v_pk_fma_f32 v[92:93], v[240:241], v[196:197], v[92:93]
	v_pk_fma_f32 v[94:95], v[242:243], v[198:199], v[94:95]
	v_pk_add_f32 v[86:87], v[86:87], v[88:89]
	v_pk_fma_f32 v[92:93], v[244:245], v[200:201], v[92:93]
	v_pk_fma_f32 v[94:95], v[246:247], v[202:203], v[94:95]
	v_add_f32_e32 v86, v86, v87
	v_pk_fma_f32 v[92:93], v[248:249], v[204:205], v[92:93]
	v_rcp_f32_e32 v87, v86
	v_pk_add_f32 v[92:93], v[92:93], v[94:95]
	v_mul_f32_e32 v87, v55, v87
	v_add_f32_e32 v92, v92, v93
	v_mul_f32_e32 v109, v86, v87
	v_mul_f32_e32 v92, v92, v87
	v_mul_f32_e32 v102, 0x43800000, v87
	v_mul_f32_e32 v106, 0x3d800000, v92
	v_max3_f32 v122, v103, v105, v106
	v_cmp_gt_u32_e64 s[6:7], 16, v104
	v_mov_b32_e32 v123, v122
	s_nop 1
	v_permlane16_swap_b32_e32 v122, v123
	v_max_f32_e32 v122, v122, v123
	v_mov_b32_e32 v123, v122
	s_nop 1
	v_permlane32_swap_b32_e32 v122, v123
	v_max_f32_e32 v36, v122, v123
	v_mul_f32_e32 v123, 0x3fb8aa3b, v36
	v_fma_f32 v111, v103, v121, -v123
	v_exp_f32_e32 v111, v111
	s_nop 0
	v_mul_f32_e32 v112, v111, v100
	v_mul_f32_e32 v110, v111, v107
	v_mov_b32_e32 v114, v111
	v_pk_mul_f32 v[208:209], v[208:209], v[112:113] op_sel_hi:[1,0]
	v_pk_mul_f32 v[210:211], v[210:211], v[112:113] op_sel_hi:[1,0]
	v_pk_mul_f32 v[212:213], v[212:213], v[112:113] op_sel_hi:[1,0]
	v_pk_mul_f32 v[214:215], v[214:215], v[112:113] op_sel_hi:[1,0]
	v_pk_mul_f32 v[216:217], v[216:217], v[112:113] op_sel_hi:[1,0]
	v_pk_mul_f32 v[218:219], v[218:219], v[112:113] op_sel_hi:[1,0]
	v_pk_mul_f32 v[220:221], v[220:221], v[112:113] op_sel_hi:[1,0]
	s_waitcnt vmcnt(13)
	v_mov_b32_e32 v115, v110
	v_fma_mix_f32 v116, v110, v70, 0 op_sel_hi:[0,1,0]
	v_fma_mix_f32 v117, v110, v70, 0 op_sel:[0,1,0] op_sel_hi:[0,1,0]
	v_fma_mix_f32 v118, v110, v71, 0 op_sel_hi:[0,1,0]
	v_cvt_pk_fp8_f32 v72, v208, v209
	v_cvt_pk_fp8_f32 v73, v212, v213
	v_cvt_pk_fp8_f32 v74, v216, v217
	v_cvt_pk_fp8_f32 v75, v220, v221
	v_cvt_pk_fp8_f32 v72, v210, v211 op_sel:[0,0,1]
	v_cvt_pk_fp8_f32 v73, v214, v215 op_sel:[0,0,1]
	v_cvt_pk_fp8_f32 v74, v218, v219 op_sel:[0,0,1]
	s_nop 1
	v_mfma_f32_16x16x32_fp8_fp8 v[152:155], v[72:73], v[30:31], 0
	v_mfma_f32_16x16x32_fp8_fp8 v[152:155], v[74:75], v[32:33], v[152:155]
	v_fma_f32 v111, v105, v121, -v123
	v_exp_f32_e32 v111, v111
	s_nop 0
	v_mul_f32_e32 v112, v111, v101
	v_mul_f32_e32 v110, v111, v108
	v_add_f32_e32 v114, v114, v111
	v_pk_mul_f32 v[222:223], v[222:223], v[112:113] op_sel_hi:[1,0]
	v_pk_mul_f32 v[224:225], v[224:225], v[112:113] op_sel_hi:[1,0]
	v_pk_mul_f32 v[226:227], v[226:227], v[112:113] op_sel_hi:[1,0]
	v_pk_mul_f32 v[228:229], v[228:229], v[112:113] op_sel_hi:[1,0]
	v_pk_mul_f32 v[230:231], v[230:231], v[112:113] op_sel_hi:[1,0]
	v_pk_mul_f32 v[232:233], v[232:233], v[112:113] op_sel_hi:[1,0]
	v_pk_mul_f32 v[234:235], v[234:235], v[112:113] op_sel_hi:[1,0]
	s_waitcnt vmcnt(11)
	v_add_f32_e32 v115, v115, v110
	v_fma_mix_f32 v116, v110, v66, v116 op_sel_hi:[0,1,0]
	v_fma_mix_f32 v117, v110, v66, v117 op_sel:[0,1,0] op_sel_hi:[0,1,0]
	v_fma_mix_f32 v118, v110, v67, v118 op_sel_hi:[0,1,0]
	v_cvt_pk_fp8_f32 v76, v222, v223
	v_cvt_pk_fp8_f32 v77, v226, v227
	v_cvt_pk_fp8_f32 v78, v230, v231
	v_cvt_pk_fp8_f32 v79, v234, v235
	v_cvt_pk_fp8_f32 v76, v224, v225 op_sel:[0,0,1]
	v_cvt_pk_fp8_f32 v77, v228, v229 op_sel:[0,0,1]
	v_cvt_pk_fp8_f32 v78, v232, v233 op_sel:[0,0,1]
	s_nop 1
	v_mfma_f32_16x16x32_fp8_fp8 v[152:155], v[76:77], v[26:27], v[152:155]
	v_mfma_f32_16x16x32_fp8_fp8 v[152:155], v[78:79], v[28:29], v[152:155]
	v_fma_f32 v111, v106, v121, -v123
	v_exp_f32_e32 v111, v111
	s_nop 0
	v_mul_f32_e32 v112, v111, v102
	v_mul_f32_e32 v110, v111, v109
	v_add_f32_e32 v114, v114, v111
	v_pk_mul_f32 v[236:237], v[236:237], v[112:113] op_sel_hi:[1,0]
	v_pk_mul_f32 v[238:239], v[238:239], v[112:113] op_sel_hi:[1,0]
	v_pk_mul_f32 v[240:241], v[240:241], v[112:113] op_sel_hi:[1,0]
	v_pk_mul_f32 v[242:243], v[242:243], v[112:113] op_sel_hi:[1,0]
	v_pk_mul_f32 v[244:245], v[244:245], v[112:113] op_sel_hi:[1,0]
	v_pk_mul_f32 v[246:247], v[246:247], v[112:113] op_sel_hi:[1,0]
	v_pk_mul_f32 v[248:249], v[248:249], v[112:113] op_sel_hi:[1,0]
	s_waitcnt vmcnt(9)
	v_add_f32_e32 v115, v115, v110
	v_fma_mix_f32 v116, v110, v68, v116 op_sel_hi:[0,1,0]
	v_fma_mix_f32 v117, v110, v68, v117 op_sel:[0,1,0] op_sel_hi:[0,1,0]
	v_fma_mix_f32 v118, v110, v69, v118 op_sel_hi:[0,1,0]
	v_cvt_pk_fp8_f32 v80, v236, v237
	v_cvt_pk_fp8_f32 v81, v240, v241
	v_cvt_pk_fp8_f32 v82, v244, v245
	v_cvt_pk_fp8_f32 v83, v248, v249
	v_cvt_pk_fp8_f32 v80, v238, v239 op_sel:[0,0,1]
	v_cvt_pk_fp8_f32 v81, v242, v243 op_sel:[0,0,1]
	v_cvt_pk_fp8_f32 v82, v246, v247 op_sel:[0,0,1]
	s_nop 1
	v_mfma_f32_16x16x32_fp8_fp8 v[152:155], v[80:81], v[18:19], v[152:155]
	v_mfma_f32_16x16x32_fp8_fp8 v[152:155], v[82:83], v[20:21], v[152:155]
	v_mov_b32_e32 v86, v114
	v_mov_b32_e32 v87, v115
	v_mov_b32_e32 v88, v116
	v_mov_b32_e32 v89, v117
	v_mov_b32_e32 v90, v118
	v_permlane16_swap_b32_e32 v114, v86
	v_permlane16_swap_b32_e32 v115, v87
	v_permlane16_swap_b32_e32 v116, v88
	v_permlane16_swap_b32_e32 v117, v89
	v_permlane16_swap_b32_e32 v118, v90
	v_add_f32_e32 v114, v114, v86
	v_add_f32_e32 v115, v115, v87
	v_add_f32_e32 v116, v116, v88
	v_add_f32_e32 v117, v117, v89
	v_add_f32_e32 v118, v118, v90
	v_mov_b32_e32 v86, v114
	v_mov_b32_e32 v87, v115
	v_mov_b32_e32 v88, v116
	v_mov_b32_e32 v89, v117
	v_mov_b32_e32 v90, v118
	v_permlane32_swap_b32_e32 v114, v86
	v_permlane32_swap_b32_e32 v115, v87
	v_permlane32_swap_b32_e32 v116, v88
	v_permlane32_swap_b32_e32 v117, v89
	v_permlane32_swap_b32_e32 v118, v90
	v_add_f32_e32 v37, v114, v86
	v_add_f32_e32 v20, v115, v87
	v_add_f32_e32 v18, v116, v88
	v_add_f32_e32 v19, v117, v89
	v_add_f32_e32 v21, v118, v90
	ds_write2_b32 v156, v152, v153 offset0:0 offset1:20
	ds_write2_b32 v156, v154, v155 offset0:40 offset1:60
